# v110 + exact vmcnt count in MoE odd halves when next tile is full (4 A-DMAs outstanding): two copies of the odd full path
# speedup vs baseline: 1.0113x; 1.0113x over previous
.LBB0_732:
	s_cmp_lg_u64 s[2:3], 0
	s_cbranch_scc1 .Lswp_guO_half
	s_cmp_lg_u64 s[96:97], 0
	s_cbranch_scc1 .Locnt_gu_two
	ds_read_b64_tr_b16 v[162:163], v190 offset:32768
	ds_read_b64_tr_b16 v[164:165], v191 offset:32768
	ds_read_b64_tr_b16 v[170:171], v192 offset:32768
	ds_read_b64_tr_b16 v[172:173], v193 offset:32768
	ds_read_b128 v[214:217], v207 offset:32768
	ds_read_b128 v[224:227], v207 offset:34816
	ds_read_b128 v[232:235], v207 offset:36864
	ds_read_b128 v[240:243], v207 offset:38912
	ds_read_b64_tr_b16 v[166:167], v190 offset:40960
	ds_read_b64_tr_b16 v[168:169], v191 offset:40960
	ds_read_b64_tr_b16 v[174:175], v192 offset:40960
	ds_read_b64_tr_b16 v[176:177], v193 offset:40960
	ds_read_b128 v[218:221], v207 offset:33792
	ds_read_b128 v[228:231], v207 offset:35840
	ds_read_b128 v[236:239], v207 offset:37888
	ds_read_b128 v[244:247], v207 offset:39936
	s_lshl_b64 s[2:3], s[38:39], 18
	s_add_u32 s4, s2, 0x40000
	s_addc_u32 s5, s3, 0
	s_add_u32 s2, s67, s4
	s_addc_u32 s3, s66, s5
	s_add_u32 s4, s35, s4
	s_addc_u32 s5, s34, s5
	s_add_i32 s94, s17, 2
	s_ashr_i32 s95, s94, 31
	s_lshl_b64 s[94:95], s[94:95], 7
	s_add_u32 s94, s8, s94
	s_addc_u32 s95, s9, s95
	s_add_u32 s94, s94, 0x80
	s_addc_u32 s95, s95, 0
	v_lshl_add_u64 v[250:251], s[94:95], 0, v[178:179]
	v_lshl_add_u64 v[252:253], s[94:95], 0, v[180:181]
	v_lshl_add_u64 v[222:223], s[94:95], 0, v[182:183]
	s_setprio 1
	s_waitcnt lgkmcnt(11)
	v_mfma_f32_16x16x32_bf16 v[158:161], v[162:165], v[214:217], v[158:161]
	v_mfma_f32_16x16x32_bf16 v[154:157], v[170:173], v[214:217], v[154:157]
	s_waitcnt lgkmcnt(10)
	v_mfma_f32_16x16x32_bf16 v[146:149], v[162:165], v[224:227], v[146:149]
	v_mfma_f32_16x16x32_bf16 v[138:141], v[170:173], v[224:227], v[138:141]
	s_waitcnt lgkmcnt(9)
	v_mfma_f32_16x16x32_bf16 v[130:133], v[162:165], v[232:235], v[130:133]
	v_mfma_f32_16x16x32_bf16 v[122:125], v[170:173], v[232:235], v[122:125]
	s_waitcnt lgkmcnt(8)
	v_mfma_f32_16x16x32_bf16 v[114:117], v[162:165], v[240:243], v[114:117]
	v_mfma_f32_16x16x32_bf16 v[106:109], v[170:173], v[240:243], v[106:109]
	ds_read_b64_tr_b16 v[162:163], v190 offset:49152
	ds_read_b64_tr_b16 v[164:165], v191 offset:49152
	ds_read_b64_tr_b16 v[170:171], v192 offset:49152
	ds_read_b64_tr_b16 v[172:173], v193 offset:49152
	s_waitcnt lgkmcnt(7)
	v_mfma_f32_16x16x32_bf16 v[158:161], v[166:169], v[218:221], v[158:161]
	v_mfma_f32_16x16x32_bf16 v[154:157], v[174:177], v[218:221], v[154:157]
	s_waitcnt lgkmcnt(6)
	v_mfma_f32_16x16x32_bf16 v[146:149], v[166:169], v[228:231], v[146:149]
	v_mfma_f32_16x16x32_bf16 v[138:141], v[174:177], v[228:231], v[138:141]
	s_waitcnt lgkmcnt(5)
	v_mfma_f32_16x16x32_bf16 v[130:133], v[166:169], v[236:239], v[130:133]
	v_mfma_f32_16x16x32_bf16 v[122:125], v[174:177], v[236:239], v[122:125]
	s_waitcnt lgkmcnt(4)
	v_mfma_f32_16x16x32_bf16 v[114:117], v[166:169], v[244:247], v[114:117]
	v_mfma_f32_16x16x32_bf16 v[106:109], v[174:177], v[244:247], v[106:109]
	ds_read_b64_tr_b16 v[166:167], v190 offset:57344
	ds_read_b64_tr_b16 v[168:169], v191 offset:57344
	ds_read_b64_tr_b16 v[174:175], v192 offset:57344
	ds_read_b64_tr_b16 v[176:177], v193 offset:57344
	s_waitcnt lgkmcnt(4)
	v_mfma_f32_16x16x32_bf16 v[150:153], v[162:165], v[214:217], v[150:153]
	v_mfma_f32_16x16x32_bf16 v[142:145], v[170:173], v[214:217], v[142:145]
	ds_read_b128 v[214:217], v207 offset:49152
	v_mfma_f32_16x16x32_bf16 v[134:137], v[162:165], v[224:227], v[134:137]
	v_mfma_f32_16x16x32_bf16 v[126:129], v[170:173], v[224:227], v[126:129]
	ds_read_b128 v[224:227], v207 offset:51200
	v_mfma_f32_16x16x32_bf16 v[118:121], v[162:165], v[232:235], v[118:121]
	v_mfma_f32_16x16x32_bf16 v[110:113], v[170:173], v[232:235], v[110:113]
	ds_read_b128 v[232:235], v207 offset:53248
	v_mfma_f32_16x16x32_bf16 v[102:105], v[162:165], v[240:243], v[102:105]
	v_mfma_f32_16x16x32_bf16 v[98:101], v[170:173], v[240:243], v[98:101]
	ds_read_b128 v[240:243], v207 offset:55296
	ds_read_b64_tr_b16 v[162:163], v190 offset:32768
	ds_read_b64_tr_b16 v[164:165], v191 offset:32768
	ds_read_b64_tr_b16 v[170:171], v192 offset:32768
	ds_read_b64_tr_b16 v[172:173], v193 offset:32768
	s_waitcnt lgkmcnt(8)
	v_mfma_f32_16x16x32_bf16 v[150:153], v[166:169], v[218:221], v[150:153]
	v_mfma_f32_16x16x32_bf16 v[142:145], v[174:177], v[218:221], v[142:145]
	ds_read_b128 v[218:221], v207 offset:50176
	v_mfma_f32_16x16x32_bf16 v[134:137], v[166:169], v[228:231], v[134:137]
	v_mfma_f32_16x16x32_bf16 v[126:129], v[174:177], v[228:231], v[126:129]
	ds_read_b128 v[228:231], v207 offset:52224
	v_mfma_f32_16x16x32_bf16 v[118:121], v[166:169], v[236:239], v[118:121]
	v_mfma_f32_16x16x32_bf16 v[110:113], v[174:177], v[236:239], v[110:113]
	ds_read_b128 v[236:239], v207 offset:54272
	v_mfma_f32_16x16x32_bf16 v[102:105], v[166:169], v[244:247], v[102:105]
	v_mfma_f32_16x16x32_bf16 v[98:101], v[174:177], v[244:247], v[98:101]
	ds_read_b128 v[244:247], v207 offset:56320
	ds_read_b64_tr_b16 v[166:167], v190 offset:40960
	ds_read_b64_tr_b16 v[168:169], v191 offset:40960
	ds_read_b64_tr_b16 v[174:175], v192 offset:40960
	ds_read_b64_tr_b16 v[176:177], v193 offset:40960
	s_waitcnt lgkmcnt(8)
	v_mfma_f32_16x16x32_bf16 v[94:97], v[162:165], v[214:217], v[94:97]
	v_mfma_f32_16x16x32_bf16 v[86:89], v[170:173], v[214:217], v[86:89]
	v_mfma_f32_16x16x32_bf16 v[78:81], v[162:165], v[224:227], v[78:81]
	v_mfma_f32_16x16x32_bf16 v[70:73], v[170:173], v[224:227], v[70:73]
	v_mfma_f32_16x16x32_bf16 v[62:65], v[162:165], v[232:235], v[62:65]
	v_mfma_f32_16x16x32_bf16 v[54:57], v[170:173], v[232:235], v[54:57]
	v_mfma_f32_16x16x32_bf16 v[46:49], v[162:165], v[240:243], v[46:49]
	v_mfma_f32_16x16x32_bf16 v[38:41], v[170:173], v[240:243], v[38:41]
	ds_read_b64_tr_b16 v[162:163], v190 offset:49152
	ds_read_b64_tr_b16 v[164:165], v191 offset:49152
	ds_read_b64_tr_b16 v[170:171], v192 offset:49152
	ds_read_b64_tr_b16 v[172:173], v193 offset:49152
	s_waitcnt lgkmcnt(4)
	v_mfma_f32_16x16x32_bf16 v[94:97], v[166:169], v[218:221], v[94:97]
	v_mfma_f32_16x16x32_bf16 v[86:89], v[174:177], v[218:221], v[86:89]
	v_mfma_f32_16x16x32_bf16 v[78:81], v[166:169], v[228:231], v[78:81]
	v_mfma_f32_16x16x32_bf16 v[70:73], v[174:177], v[228:231], v[70:73]
	v_mfma_f32_16x16x32_bf16 v[62:65], v[166:169], v[236:239], v[62:65]
	v_mfma_f32_16x16x32_bf16 v[54:57], v[174:177], v[236:239], v[54:57]
	v_mfma_f32_16x16x32_bf16 v[46:49], v[166:169], v[244:247], v[46:49]
	v_mfma_f32_16x16x32_bf16 v[38:41], v[174:177], v[244:247], v[38:41]
	ds_read_b64_tr_b16 v[166:167], v190 offset:57344
	ds_read_b64_tr_b16 v[168:169], v191 offset:57344
	ds_read_b64_tr_b16 v[174:175], v192 offset:57344
	ds_read_b64_tr_b16 v[176:177], v193 offset:57344
	s_waitcnt lgkmcnt(4)
	v_mfma_f32_16x16x32_bf16 v[90:93], v[162:165], v[214:217], v[90:93]
	v_mfma_f32_16x16x32_bf16 v[82:85], v[170:173], v[214:217], v[82:85]
	s_waitcnt vmcnt(11)
	v_cvt_pk_bf16_f32 v248, v2, v3
	v_cvt_pk_bf16_f32 v249, v4, v5
	ds_write_b64 v197, v[248:249] offset:16384
	global_load_dwordx4 v[2:5], v189, s[2:3]
	v_mfma_f32_16x16x32_bf16 v[74:77], v[162:165], v[224:227], v[74:77]
	v_mfma_f32_16x16x32_bf16 v[66:69], v[170:173], v[224:227], v[66:69]
	s_waitcnt vmcnt(11)
	v_cvt_pk_bf16_f32 v248, v6, v7
	v_cvt_pk_bf16_f32 v249, v8, v9
	ds_write_b64 v196, v[248:249] offset:16384
	global_load_dwordx4 v[6:9], v189, s[4:5]
	v_mfma_f32_16x16x32_bf16 v[58:61], v[162:165], v[232:235], v[58:61]
	v_mfma_f32_16x16x32_bf16 v[50:53], v[170:173], v[232:235], v[50:53]
	s_waitcnt vmcnt(11)
	v_cvt_pk_bf16_f32 v248, v10, v11
	v_cvt_pk_bf16_f32 v249, v12, v13
	ds_write_b64 v197, v[248:249]
	s_add_u32 s98, s2, 0x2000
	s_addc_u32 s99, s3, 0
	global_load_dwordx4 v[10:13], v189, s[98:99]
	v_mfma_f32_16x16x32_bf16 v[42:45], v[162:165], v[240:243], v[42:45]
	v_mfma_f32_16x16x32_bf16 v[30:33], v[170:173], v[240:243], v[30:33]
	s_waitcnt vmcnt(11)
	v_cvt_pk_bf16_f32 v248, v14, v15
	v_cvt_pk_bf16_f32 v249, v16, v17
	ds_write_b64 v195, v[248:249] offset:16384
	s_add_u32 s100, s4, 0x2000
	s_addc_u32 s101, s5, 0
	global_load_dwordx4 v[14:17], v189, s[100:101]
	s_waitcnt lgkmcnt(4)
	v_mfma_f32_16x16x32_bf16 v[90:93], v[166:169], v[218:221], v[90:93]
	v_mfma_f32_16x16x32_bf16 v[82:85], v[174:177], v[218:221], v[82:85]
	s_waitcnt vmcnt(11)
	v_cvt_pk_bf16_f32 v248, v18, v19
	v_cvt_pk_bf16_f32 v249, v20, v21
	ds_write_b64 v196, v[248:249]
	s_add_u32 s98, s2, 0x4000
	s_addc_u32 s99, s3, 0
	global_load_dwordx4 v[18:21], v189, s[98:99]
	v_mfma_f32_16x16x32_bf16 v[74:77], v[166:169], v[228:231], v[74:77]
	v_mfma_f32_16x16x32_bf16 v[66:69], v[174:177], v[228:231], v[66:69]
	s_waitcnt vmcnt(11)
	v_cvt_pk_bf16_f32 v248, v22, v23
	v_cvt_pk_bf16_f32 v249, v24, v25
	ds_write_b64 v194, v[248:249] offset:16384
	s_add_u32 s100, s4, 0x4000
	s_addc_u32 s101, s5, 0
	global_load_dwordx4 v[22:25], v189, s[100:101]
	v_mfma_f32_16x16x32_bf16 v[58:61], v[166:169], v[236:239], v[58:61]
	v_mfma_f32_16x16x32_bf16 v[50:53], v[174:177], v[236:239], v[50:53]
	s_waitcnt vmcnt(11)
	v_cvt_pk_bf16_f32 v248, v26, v27
	v_cvt_pk_bf16_f32 v249, v28, v29
	ds_write_b64 v195, v[248:249]
	s_add_u32 s98, s2, 0x6000
	s_addc_u32 s99, s3, 0
	global_load_dwordx4 v[26:29], v189, s[98:99]
	v_mfma_f32_16x16x32_bf16 v[42:45], v[166:169], v[244:247], v[42:45]
	v_mfma_f32_16x16x32_bf16 v[30:33], v[174:177], v[244:247], v[30:33]
	s_waitcnt vmcnt(11)
	v_cvt_pk_bf16_f32 v248, v34, v35
	v_cvt_pk_bf16_f32 v249, v36, v37
	ds_write_b64 v194, v[248:249]
	s_add_u32 s100, s4, 0x6000
	s_addc_u32 s101, s5, 0
	global_load_dwordx4 v[34:37], v189, s[100:101]
	v_lshl_add_u64 v[248:249], s[94:95], 0, v[184:185]
	s_setprio 0

.Locnt_gu_two:
	ds_read_b64_tr_b16 v[162:163], v190 offset:32768
	ds_read_b64_tr_b16 v[164:165], v191 offset:32768
	ds_read_b64_tr_b16 v[170:171], v192 offset:32768
	ds_read_b64_tr_b16 v[172:173], v193 offset:32768
	ds_read_b128 v[214:217], v207 offset:32768
	ds_read_b128 v[224:227], v207 offset:34816
	ds_read_b128 v[232:235], v207 offset:36864
	ds_read_b128 v[240:243], v207 offset:38912
	ds_read_b64_tr_b16 v[166:167], v190 offset:40960
	ds_read_b64_tr_b16 v[168:169], v191 offset:40960
	ds_read_b64_tr_b16 v[174:175], v192 offset:40960
	ds_read_b64_tr_b16 v[176:177], v193 offset:40960
	ds_read_b128 v[218:221], v207 offset:33792
	ds_read_b128 v[228:231], v207 offset:35840
	ds_read_b128 v[236:239], v207 offset:37888
	ds_read_b128 v[244:247], v207 offset:39936
	s_lshl_b64 s[2:3], s[38:39], 18
	s_add_u32 s4, s2, 0x40000
	s_addc_u32 s5, s3, 0
	s_add_u32 s2, s67, s4
	s_addc_u32 s3, s66, s5
	s_add_u32 s4, s35, s4
	s_addc_u32 s5, s34, s5
	s_add_i32 s94, s17, 2
	s_ashr_i32 s95, s94, 31
	s_lshl_b64 s[94:95], s[94:95], 7
	s_add_u32 s94, s8, s94
	s_addc_u32 s95, s9, s95
	s_add_u32 s94, s94, 0x80
	s_addc_u32 s95, s95, 0
	v_lshl_add_u64 v[250:251], s[94:95], 0, v[178:179]
	v_lshl_add_u64 v[252:253], s[94:95], 0, v[180:181]
	v_lshl_add_u64 v[222:223], s[94:95], 0, v[182:183]
	s_setprio 1
	s_waitcnt lgkmcnt(11)
	v_mfma_f32_16x16x32_bf16 v[158:161], v[162:165], v[214:217], v[158:161]
	v_mfma_f32_16x16x32_bf16 v[154:157], v[170:173], v[214:217], v[154:157]
	s_waitcnt lgkmcnt(10)
	v_mfma_f32_16x16x32_bf16 v[146:149], v[162:165], v[224:227], v[146:149]
	v_mfma_f32_16x16x32_bf16 v[138:141], v[170:173], v[224:227], v[138:141]
	s_waitcnt lgkmcnt(9)
	v_mfma_f32_16x16x32_bf16 v[130:133], v[162:165], v[232:235], v[130:133]
	v_mfma_f32_16x16x32_bf16 v[122:125], v[170:173], v[232:235], v[122:125]
	s_waitcnt lgkmcnt(8)
	v_mfma_f32_16x16x32_bf16 v[114:117], v[162:165], v[240:243], v[114:117]
	v_mfma_f32_16x16x32_bf16 v[106:109], v[170:173], v[240:243], v[106:109]
	ds_read_b64_tr_b16 v[162:163], v190 offset:49152
	ds_read_b64_tr_b16 v[164:165], v191 offset:49152
	ds_read_b64_tr_b16 v[170:171], v192 offset:49152
	ds_read_b64_tr_b16 v[172:173], v193 offset:49152
	s_waitcnt lgkmcnt(7)
	v_mfma_f32_16x16x32_bf16 v[158:161], v[166:169], v[218:221], v[158:161]
	v_mfma_f32_16x16x32_bf16 v[154:157], v[174:177], v[218:221], v[154:157]
	s_waitcnt lgkmcnt(6)
	v_mfma_f32_16x16x32_bf16 v[146:149], v[166:169], v[228:231], v[146:149]
	v_mfma_f32_16x16x32_bf16 v[138:141], v[174:177], v[228:231], v[138:141]
	s_waitcnt lgkmcnt(5)
	v_mfma_f32_16x16x32_bf16 v[130:133], v[166:169], v[236:239], v[130:133]
	v_mfma_f32_16x16x32_bf16 v[122:125], v[174:177], v[236:239], v[122:125]
	s_waitcnt lgkmcnt(4)
	v_mfma_f32_16x16x32_bf16 v[114:117], v[166:169], v[244:247], v[114:117]
	v_mfma_f32_16x16x32_bf16 v[106:109], v[174:177], v[244:247], v[106:109]
	ds_read_b64_tr_b16 v[166:167], v190 offset:57344
	ds_read_b64_tr_b16 v[168:169], v191 offset:57344
	ds_read_b64_tr_b16 v[174:175], v192 offset:57344
	ds_read_b64_tr_b16 v[176:177], v193 offset:57344
	s_waitcnt lgkmcnt(4)
	v_mfma_f32_16x16x32_bf16 v[150:153], v[162:165], v[214:217], v[150:153]
	v_mfma_f32_16x16x32_bf16 v[142:145], v[170:173], v[214:217], v[142:145]
	ds_read_b128 v[214:217], v207 offset:49152
	v_mfma_f32_16x16x32_bf16 v[134:137], v[162:165], v[224:227], v[134:137]
	v_mfma_f32_16x16x32_bf16 v[126:129], v[170:173], v[224:227], v[126:129]
	ds_read_b128 v[224:227], v207 offset:51200
	v_mfma_f32_16x16x32_bf16 v[118:121], v[162:165], v[232:235], v[118:121]
	v_mfma_f32_16x16x32_bf16 v[110:113], v[170:173], v[232:235], v[110:113]
	ds_read_b128 v[232:235], v207 offset:53248
	v_mfma_f32_16x16x32_bf16 v[102:105], v[162:165], v[240:243], v[102:105]
	v_mfma_f32_16x16x32_bf16 v[98:101], v[170:173], v[240:243], v[98:101]
	ds_read_b128 v[240:243], v207 offset:55296
	ds_read_b64_tr_b16 v[162:163], v190 offset:32768
	ds_read_b64_tr_b16 v[164:165], v191 offset:32768
	ds_read_b64_tr_b16 v[170:171], v192 offset:32768
	ds_read_b64_tr_b16 v[172:173], v193 offset:32768
	s_waitcnt lgkmcnt(8)
	v_mfma_f32_16x16x32_bf16 v[150:153], v[166:169], v[218:221], v[150:153]
	v_mfma_f32_16x16x32_bf16 v[142:145], v[174:177], v[218:221], v[142:145]
	ds_read_b128 v[218:221], v207 offset:50176
	v_mfma_f32_16x16x32_bf16 v[134:137], v[166:169], v[228:231], v[134:137]
	v_mfma_f32_16x16x32_bf16 v[126:129], v[174:177], v[228:231], v[126:129]
	ds_read_b128 v[228:231], v207 offset:52224
	v_mfma_f32_16x16x32_bf16 v[118:121], v[166:169], v[236:239], v[118:121]
	v_mfma_f32_16x16x32_bf16 v[110:113], v[174:177], v[236:239], v[110:113]
	ds_read_b128 v[236:239], v207 offset:54272
	v_mfma_f32_16x16x32_bf16 v[102:105], v[166:169], v[244:247], v[102:105]
	v_mfma_f32_16x16x32_bf16 v[98:101], v[174:177], v[244:247], v[98:101]
	ds_read_b128 v[244:247], v207 offset:56320
	ds_read_b64_tr_b16 v[166:167], v190 offset:40960
	ds_read_b64_tr_b16 v[168:169], v191 offset:40960
	ds_read_b64_tr_b16 v[174:175], v192 offset:40960
	ds_read_b64_tr_b16 v[176:177], v193 offset:40960
	s_waitcnt lgkmcnt(8)
	v_mfma_f32_16x16x32_bf16 v[94:97], v[162:165], v[214:217], v[94:97]
	v_mfma_f32_16x16x32_bf16 v[86:89], v[170:173], v[214:217], v[86:89]
	v_mfma_f32_16x16x32_bf16 v[78:81], v[162:165], v[224:227], v[78:81]
	v_mfma_f32_16x16x32_bf16 v[70:73], v[170:173], v[224:227], v[70:73]
	v_mfma_f32_16x16x32_bf16 v[62:65], v[162:165], v[232:235], v[62:65]
	v_mfma_f32_16x16x32_bf16 v[54:57], v[170:173], v[232:235], v[54:57]
	v_mfma_f32_16x16x32_bf16 v[46:49], v[162:165], v[240:243], v[46:49]
	v_mfma_f32_16x16x32_bf16 v[38:41], v[170:173], v[240:243], v[38:41]
	ds_read_b64_tr_b16 v[162:163], v190 offset:49152
	ds_read_b64_tr_b16 v[164:165], v191 offset:49152
	ds_read_b64_tr_b16 v[170:171], v192 offset:49152
	ds_read_b64_tr_b16 v[172:173], v193 offset:49152
	s_waitcnt lgkmcnt(4)
	v_mfma_f32_16x16x32_bf16 v[94:97], v[166:169], v[218:221], v[94:97]
	v_mfma_f32_16x16x32_bf16 v[86:89], v[174:177], v[218:221], v[86:89]
	v_mfma_f32_16x16x32_bf16 v[78:81], v[166:169], v[228:231], v[78:81]
	v_mfma_f32_16x16x32_bf16 v[70:73], v[174:177], v[228:231], v[70:73]
	v_mfma_f32_16x16x32_bf16 v[62:65], v[166:169], v[236:239], v[62:65]
	v_mfma_f32_16x16x32_bf16 v[54:57], v[174:177], v[236:239], v[54:57]
	v_mfma_f32_16x16x32_bf16 v[46:49], v[166:169], v[244:247], v[46:49]
	v_mfma_f32_16x16x32_bf16 v[38:41], v[174:177], v[244:247], v[38:41]
	ds_read_b64_tr_b16 v[166:167], v190 offset:57344
	ds_read_b64_tr_b16 v[168:169], v191 offset:57344
	ds_read_b64_tr_b16 v[174:175], v192 offset:57344
	ds_read_b64_tr_b16 v[176:177], v193 offset:57344
	s_waitcnt lgkmcnt(4)
	v_mfma_f32_16x16x32_bf16 v[90:93], v[162:165], v[214:217], v[90:93]
	v_mfma_f32_16x16x32_bf16 v[82:85], v[170:173], v[214:217], v[82:85]
	s_waitcnt vmcnt(9)
	v_cvt_pk_bf16_f32 v248, v2, v3
	v_cvt_pk_bf16_f32 v249, v4, v5
	ds_write_b64 v197, v[248:249] offset:16384
	global_load_dwordx4 v[2:5], v189, s[2:3]
	v_mfma_f32_16x16x32_bf16 v[74:77], v[162:165], v[224:227], v[74:77]
	v_mfma_f32_16x16x32_bf16 v[66:69], v[170:173], v[224:227], v[66:69]
	s_waitcnt vmcnt(9)
	v_cvt_pk_bf16_f32 v248, v6, v7
	v_cvt_pk_bf16_f32 v249, v8, v9
	ds_write_b64 v196, v[248:249] offset:16384
	global_load_dwordx4 v[6:9], v189, s[4:5]
	v_mfma_f32_16x16x32_bf16 v[58:61], v[162:165], v[232:235], v[58:61]
	v_mfma_f32_16x16x32_bf16 v[50:53], v[170:173], v[232:235], v[50:53]
	s_waitcnt vmcnt(9)
	v_cvt_pk_bf16_f32 v248, v10, v11
	v_cvt_pk_bf16_f32 v249, v12, v13
	ds_write_b64 v197, v[248:249]
	s_add_u32 s98, s2, 0x2000
	s_addc_u32 s99, s3, 0
	global_load_dwordx4 v[10:13], v189, s[98:99]
	v_mfma_f32_16x16x32_bf16 v[42:45], v[162:165], v[240:243], v[42:45]
	v_mfma_f32_16x16x32_bf16 v[30:33], v[170:173], v[240:243], v[30:33]
	s_waitcnt vmcnt(9)
	v_cvt_pk_bf16_f32 v248, v14, v15
	v_cvt_pk_bf16_f32 v249, v16, v17
	ds_write_b64 v195, v[248:249] offset:16384
	s_add_u32 s100, s4, 0x2000
	s_addc_u32 s101, s5, 0
	global_load_dwordx4 v[14:17], v189, s[100:101]
	s_waitcnt lgkmcnt(4)
	v_mfma_f32_16x16x32_bf16 v[90:93], v[166:169], v[218:221], v[90:93]
	v_mfma_f32_16x16x32_bf16 v[82:85], v[174:177], v[218:221], v[82:85]
	s_waitcnt vmcnt(9)
	v_cvt_pk_bf16_f32 v248, v18, v19
	v_cvt_pk_bf16_f32 v249, v20, v21
	ds_write_b64 v196, v[248:249]
	s_add_u32 s98, s2, 0x4000
	s_addc_u32 s99, s3, 0
	global_load_dwordx4 v[18:21], v189, s[98:99]
	v_mfma_f32_16x16x32_bf16 v[74:77], v[166:169], v[228:231], v[74:77]
	v_mfma_f32_16x16x32_bf16 v[66:69], v[174:177], v[228:231], v[66:69]
	s_waitcnt vmcnt(9)
	v_cvt_pk_bf16_f32 v248, v22, v23
	v_cvt_pk_bf16_f32 v249, v24, v25
	ds_write_b64 v194, v[248:249] offset:16384
	s_add_u32 s100, s4, 0x4000
	s_addc_u32 s101, s5, 0
	global_load_dwordx4 v[22:25], v189, s[100:101]
	v_mfma_f32_16x16x32_bf16 v[58:61], v[166:169], v[236:239], v[58:61]
	v_mfma_f32_16x16x32_bf16 v[50:53], v[174:177], v[236:239], v[50:53]
	s_waitcnt vmcnt(9)
	v_cvt_pk_bf16_f32 v248, v26, v27
	v_cvt_pk_bf16_f32 v249, v28, v29
	ds_write_b64 v195, v[248:249]
	s_add_u32 s98, s2, 0x6000
	s_addc_u32 s99, s3, 0
	global_load_dwordx4 v[26:29], v189, s[98:99]
	v_mfma_f32_16x16x32_bf16 v[42:45], v[166:169], v[244:247], v[42:45]
	v_mfma_f32_16x16x32_bf16 v[30:33], v[174:177], v[244:247], v[30:33]
	s_waitcnt vmcnt(9)
	v_cvt_pk_bf16_f32 v248, v34, v35
	v_cvt_pk_bf16_f32 v249, v36, v37
	ds_write_b64 v194, v[248:249]
	s_add_u32 s100, s4, 0x6000
	s_addc_u32 s101, s5, 0
	global_load_dwordx4 v[34:37], v189, s[100:101]
	v_lshl_add_u64 v[248:249], s[94:95], 0, v[184:185]
	s_setprio 0
	s_branch .Lswp_guO_tail

.LBB0_864:
	s_cmp_lg_u64 s[2:3], 0
	s_cbranch_scc1 .Lswp_dnO_half
	s_cmp_lg_u64 s[96:97], 0
	s_cbranch_scc1 .Locnt_dn_two
	ds_read_b64_tr_b16 v[164:165], v190 offset:32768
	ds_read_b64_tr_b16 v[166:167], v191 offset:32768
	ds_read_b64_tr_b16 v[172:173], v192 offset:32768
	ds_read_b64_tr_b16 v[174:175], v193 offset:32768
	ds_read_b128 v[210:213], v207 offset:32768
	ds_read_b128 v[218:221], v207 offset:34816
	ds_read_b128 v[228:231], v207 offset:36864
	ds_read_b128 v[236:239], v207 offset:38912
	ds_read_b64_tr_b16 v[168:169], v190 offset:40960
	ds_read_b64_tr_b16 v[170:171], v191 offset:40960
	ds_read_b64_tr_b16 v[176:177], v192 offset:40960
	ds_read_b64_tr_b16 v[178:179], v193 offset:40960
	ds_read_b128 v[214:217], v207 offset:33792
	ds_read_b128 v[224:227], v207 offset:35840
	ds_read_b128 v[232:235], v207 offset:37888
	ds_read_b128 v[240:243], v207 offset:39936
	s_lshl_b64 s[2:3], s[48:49], 19
	s_add_u32 s48, s2, 0x80000
	s_addc_u32 s49, s3, 0
	s_add_u32 s2, s74, s48
	s_addc_u32 s3, s43, s49
	s_add_u32 s48, s37, s48
	s_addc_u32 s49, s35, s49
	s_add_i32 s94, s34, 2
	s_ashr_i32 s95, s94, 31
	s_lshl_b64 s[94:95], s[94:95], 7
	s_add_u32 s94, s22, s94
	s_addc_u32 s95, s23, s95
	s_add_u32 s94, s94, 0x80
	s_addc_u32 s95, s95, 0
	v_lshl_add_u64 v[250:251], s[94:95], 0, v[180:181]
	v_lshl_add_u64 v[252:253], s[94:95], 0, v[182:183]
	v_lshl_add_u64 v[222:223], s[94:95], 0, v[184:185]
	v_lshl_add_u64 v[246:247], s[94:95], 0, v[186:187]
	s_setprio 1
	s_waitcnt lgkmcnt(11)
	v_mfma_f32_16x16x32_bf16 v[160:163], v[164:167], v[210:213], v[160:163]
	v_mfma_f32_16x16x32_bf16 v[156:159], v[172:175], v[210:213], v[156:159]
	s_waitcnt lgkmcnt(10)
	v_mfma_f32_16x16x32_bf16 v[152:155], v[164:167], v[218:221], v[152:155]
	v_mfma_f32_16x16x32_bf16 v[148:151], v[172:175], v[218:221], v[148:151]
	s_waitcnt lgkmcnt(9)
	v_mfma_f32_16x16x32_bf16 v[136:139], v[164:167], v[228:231], v[136:139]
	v_mfma_f32_16x16x32_bf16 v[132:135], v[172:175], v[228:231], v[132:135]
	s_waitcnt lgkmcnt(8)
	v_mfma_f32_16x16x32_bf16 v[120:123], v[164:167], v[236:239], v[120:123]
	v_mfma_f32_16x16x32_bf16 v[116:119], v[172:175], v[236:239], v[116:119]
	ds_read_b64_tr_b16 v[164:165], v190 offset:49152
	ds_read_b64_tr_b16 v[166:167], v191 offset:49152
	ds_read_b64_tr_b16 v[172:173], v192 offset:49152
	ds_read_b64_tr_b16 v[174:175], v193 offset:49152
	s_waitcnt lgkmcnt(7)
	v_mfma_f32_16x16x32_bf16 v[160:163], v[168:171], v[214:217], v[160:163]
	v_mfma_f32_16x16x32_bf16 v[156:159], v[176:179], v[214:217], v[156:159]
	s_waitcnt lgkmcnt(6)
	v_mfma_f32_16x16x32_bf16 v[152:155], v[168:171], v[224:227], v[152:155]
	v_mfma_f32_16x16x32_bf16 v[148:151], v[176:179], v[224:227], v[148:151]
	s_waitcnt lgkmcnt(5)
	v_mfma_f32_16x16x32_bf16 v[136:139], v[168:171], v[232:235], v[136:139]
	v_mfma_f32_16x16x32_bf16 v[132:135], v[176:179], v[232:235], v[132:135]
	s_waitcnt lgkmcnt(4)
	v_mfma_f32_16x16x32_bf16 v[120:123], v[168:171], v[240:243], v[120:123]
	v_mfma_f32_16x16x32_bf16 v[116:119], v[176:179], v[240:243], v[116:119]
	ds_read_b64_tr_b16 v[168:169], v190 offset:57344
	ds_read_b64_tr_b16 v[170:171], v191 offset:57344
	ds_read_b64_tr_b16 v[176:177], v192 offset:57344
	ds_read_b64_tr_b16 v[178:179], v193 offset:57344
	s_waitcnt lgkmcnt(4)
	v_mfma_f32_16x16x32_bf16 v[144:147], v[164:167], v[210:213], v[144:147]
	v_mfma_f32_16x16x32_bf16 v[140:143], v[172:175], v[210:213], v[140:143]
	ds_read_b128 v[210:213], v207 offset:49152
	v_mfma_f32_16x16x32_bf16 v[128:131], v[164:167], v[218:221], v[128:131]
	v_mfma_f32_16x16x32_bf16 v[124:127], v[172:175], v[218:221], v[124:127]
	ds_read_b128 v[218:221], v207 offset:51200
	v_mfma_f32_16x16x32_bf16 v[112:115], v[164:167], v[228:231], v[112:115]
	v_mfma_f32_16x16x32_bf16 v[108:111], v[172:175], v[228:231], v[108:111]
	ds_read_b128 v[228:231], v207 offset:53248
	v_mfma_f32_16x16x32_bf16 v[104:107], v[164:167], v[236:239], v[104:107]
	v_mfma_f32_16x16x32_bf16 v[100:103], v[172:175], v[236:239], v[100:103]
	ds_read_b128 v[236:239], v207 offset:55296
	ds_read_b64_tr_b16 v[164:165], v190 offset:32768
	ds_read_b64_tr_b16 v[166:167], v191 offset:32768
	ds_read_b64_tr_b16 v[172:173], v192 offset:32768
	ds_read_b64_tr_b16 v[174:175], v193 offset:32768
	s_waitcnt lgkmcnt(8)
	v_mfma_f32_16x16x32_bf16 v[144:147], v[168:171], v[214:217], v[144:147]
	v_mfma_f32_16x16x32_bf16 v[140:143], v[176:179], v[214:217], v[140:143]
	ds_read_b128 v[214:217], v207 offset:50176
	v_mfma_f32_16x16x32_bf16 v[128:131], v[168:171], v[224:227], v[128:131]
	v_mfma_f32_16x16x32_bf16 v[124:127], v[176:179], v[224:227], v[124:127]
	ds_read_b128 v[224:227], v207 offset:52224
	v_mfma_f32_16x16x32_bf16 v[112:115], v[168:171], v[232:235], v[112:115]
	v_mfma_f32_16x16x32_bf16 v[108:111], v[176:179], v[232:235], v[108:111]
	ds_read_b128 v[232:235], v207 offset:54272
	v_mfma_f32_16x16x32_bf16 v[104:107], v[168:171], v[240:243], v[104:107]
	v_mfma_f32_16x16x32_bf16 v[100:103], v[176:179], v[240:243], v[100:103]
	ds_read_b128 v[240:243], v207 offset:56320
	ds_read_b64_tr_b16 v[168:169], v190 offset:40960
	ds_read_b64_tr_b16 v[170:171], v191 offset:40960
	ds_read_b64_tr_b16 v[176:177], v192 offset:40960
	ds_read_b64_tr_b16 v[178:179], v193 offset:40960
	s_waitcnt lgkmcnt(8)
	v_mfma_f32_16x16x32_bf16 v[80:83], v[164:167], v[210:213], v[80:83]
	v_mfma_f32_16x16x32_bf16 v[68:71], v[172:175], v[210:213], v[68:71]
	v_mfma_f32_16x16x32_bf16 v[48:51], v[164:167], v[218:221], v[48:51]
	v_mfma_f32_16x16x32_bf16 v[44:47], v[172:175], v[218:221], v[44:47]
	v_mfma_f32_16x16x32_bf16 v[32:35], v[164:167], v[228:231], v[32:35]
	v_mfma_f32_16x16x32_bf16 v[28:31], v[172:175], v[228:231], v[28:31]
	v_mfma_f32_16x16x32_bf16 v[16:19], v[164:167], v[236:239], v[16:19]
	v_mfma_f32_16x16x32_bf16 v[12:15], v[172:175], v[236:239], v[12:15]
	ds_read_b64_tr_b16 v[164:165], v190 offset:49152
	ds_read_b64_tr_b16 v[166:167], v191 offset:49152
	ds_read_b64_tr_b16 v[172:173], v192 offset:49152
	ds_read_b64_tr_b16 v[174:175], v193 offset:49152
	s_waitcnt lgkmcnt(4)
	v_mfma_f32_16x16x32_bf16 v[80:83], v[168:171], v[214:217], v[80:83]
	v_mfma_f32_16x16x32_bf16 v[68:71], v[176:179], v[214:217], v[68:71]
	v_mfma_f32_16x16x32_bf16 v[48:51], v[168:171], v[224:227], v[48:51]
	v_mfma_f32_16x16x32_bf16 v[44:47], v[176:179], v[224:227], v[44:47]
	v_mfma_f32_16x16x32_bf16 v[32:35], v[168:171], v[232:235], v[32:35]
	v_mfma_f32_16x16x32_bf16 v[28:31], v[176:179], v[232:235], v[28:31]
	v_mfma_f32_16x16x32_bf16 v[16:19], v[168:171], v[240:243], v[16:19]
	v_mfma_f32_16x16x32_bf16 v[12:15], v[176:179], v[240:243], v[12:15]
	ds_read_b64_tr_b16 v[168:169], v190 offset:57344
	ds_read_b64_tr_b16 v[170:171], v191 offset:57344
	ds_read_b64_tr_b16 v[176:177], v192 offset:57344
	ds_read_b64_tr_b16 v[178:179], v193 offset:57344
	s_waitcnt lgkmcnt(4)
	v_mfma_f32_16x16x32_bf16 v[56:59], v[164:167], v[210:213], v[56:59]
	v_mfma_f32_16x16x32_bf16 v[52:55], v[172:175], v[210:213], v[52:55]
	s_waitcnt vmcnt(11)
	v_cvt_pk_bf16_f32 v244, v64, v65
	v_cvt_pk_bf16_f32 v245, v66, v67
	ds_write_b64 v196, v[244:245] offset:16384
	global_load_dwordx4 v[64:67], v189, s[2:3]
	v_mfma_f32_16x16x32_bf16 v[40:43], v[164:167], v[218:221], v[40:43]
	v_mfma_f32_16x16x32_bf16 v[36:39], v[172:175], v[218:221], v[36:39]
	s_waitcnt vmcnt(11)
	v_cvt_pk_bf16_f32 v244, v60, v61
	v_cvt_pk_bf16_f32 v245, v62, v63
	ds_write_b64 v197, v[244:245] offset:16384
	global_load_dwordx4 v[60:63], v189, s[48:49]
	v_mfma_f32_16x16x32_bf16 v[24:27], v[164:167], v[228:231], v[24:27]
	v_mfma_f32_16x16x32_bf16 v[20:23], v[172:175], v[228:231], v[20:23]
	s_waitcnt vmcnt(11)
	v_cvt_pk_bf16_f32 v244, v76, v77
	v_cvt_pk_bf16_f32 v245, v78, v79
	ds_write_b64 v195, v[244:245] offset:16384
	s_add_u32 s98, s2, 0x4000
	s_addc_u32 s99, s3, 0
	global_load_dwordx4 v[76:79], v189, s[98:99]
	v_mfma_f32_16x16x32_bf16 v[8:11], v[164:167], v[236:239], v[8:11]
	v_mfma_f32_16x16x32_bf16 v[2:5], v[172:175], v[236:239], v[4:7]
	s_waitcnt vmcnt(11)
	v_cvt_pk_bf16_f32 v244, v72, v73
	v_cvt_pk_bf16_f32 v245, v74, v75
	ds_write_b64 v197, v[244:245]
	s_add_u32 s100, s48, 0x4000
	s_addc_u32 s101, s49, 0
	global_load_dwordx4 v[72:75], v189, s[100:101]
	s_waitcnt lgkmcnt(4)
	v_mfma_f32_16x16x32_bf16 v[56:59], v[168:171], v[214:217], v[56:59]
	v_mfma_f32_16x16x32_bf16 v[52:55], v[176:179], v[214:217], v[52:55]
	s_waitcnt vmcnt(11)
	v_cvt_pk_bf16_f32 v244, v88, v89
	v_cvt_pk_bf16_f32 v245, v90, v91
	ds_write_b64 v194, v[244:245] offset:16384
	s_add_u32 s98, s2, 0x8000
	s_addc_u32 s99, s3, 0
	global_load_dwordx4 v[88:91], v189, s[98:99]
	v_mfma_f32_16x16x32_bf16 v[40:43], v[168:171], v[224:227], v[40:43]
	v_mfma_f32_16x16x32_bf16 v[36:39], v[176:179], v[224:227], v[36:39]
	s_waitcnt vmcnt(11)
	v_cvt_pk_bf16_f32 v244, v84, v85
	v_cvt_pk_bf16_f32 v245, v86, v87
	ds_write_b64 v196, v[244:245]
	s_add_u32 s100, s48, 0x8000
	s_addc_u32 s101, s49, 0
	global_load_dwordx4 v[84:87], v189, s[100:101]
	v_mfma_f32_16x16x32_bf16 v[24:27], v[168:171], v[232:235], v[24:27]
	v_mfma_f32_16x16x32_bf16 v[20:23], v[176:179], v[232:235], v[20:23]
	s_waitcnt vmcnt(11)
	v_cvt_pk_bf16_f32 v244, v96, v97
	v_cvt_pk_bf16_f32 v245, v98, v99
	ds_write_b64 v194, v[244:245]
	s_add_u32 s98, s2, 0xc000
	s_addc_u32 s99, s3, 0
	global_load_dwordx4 v[96:99], v189, s[98:99]
	v_mfma_f32_16x16x32_bf16 v[8:11], v[168:171], v[240:243], v[8:11]
	v_mfma_f32_16x16x32_bf16 v[4:7], v[176:179], v[240:243], v[2:5]
	s_waitcnt vmcnt(11)
	v_cvt_pk_bf16_f32 v244, v92, v93
	v_cvt_pk_bf16_f32 v245, v94, v95
	ds_write_b64 v195, v[244:245]
	s_add_u32 s100, s48, 0xc000
	s_addc_u32 s101, s49, 0
	global_load_dwordx4 v[92:95], v189, s[100:101]
	s_setprio 0

.Locnt_dn_two:
	ds_read_b64_tr_b16 v[164:165], v190 offset:32768
	ds_read_b64_tr_b16 v[166:167], v191 offset:32768
	ds_read_b64_tr_b16 v[172:173], v192 offset:32768
	ds_read_b64_tr_b16 v[174:175], v193 offset:32768
	ds_read_b128 v[210:213], v207 offset:32768
	ds_read_b128 v[218:221], v207 offset:34816
	ds_read_b128 v[228:231], v207 offset:36864
	ds_read_b128 v[236:239], v207 offset:38912
	ds_read_b64_tr_b16 v[168:169], v190 offset:40960
	ds_read_b64_tr_b16 v[170:171], v191 offset:40960
	ds_read_b64_tr_b16 v[176:177], v192 offset:40960
	ds_read_b64_tr_b16 v[178:179], v193 offset:40960
	ds_read_b128 v[214:217], v207 offset:33792
	ds_read_b128 v[224:227], v207 offset:35840
	ds_read_b128 v[232:235], v207 offset:37888
	ds_read_b128 v[240:243], v207 offset:39936
	s_lshl_b64 s[2:3], s[48:49], 19
	s_add_u32 s48, s2, 0x80000
	s_addc_u32 s49, s3, 0
	s_add_u32 s2, s74, s48
	s_addc_u32 s3, s43, s49
	s_add_u32 s48, s37, s48
	s_addc_u32 s49, s35, s49
	s_add_i32 s94, s34, 2
	s_ashr_i32 s95, s94, 31
	s_lshl_b64 s[94:95], s[94:95], 7
	s_add_u32 s94, s22, s94
	s_addc_u32 s95, s23, s95
	s_add_u32 s94, s94, 0x80
	s_addc_u32 s95, s95, 0
	v_lshl_add_u64 v[250:251], s[94:95], 0, v[180:181]
	v_lshl_add_u64 v[252:253], s[94:95], 0, v[182:183]
	v_lshl_add_u64 v[222:223], s[94:95], 0, v[184:185]
	v_lshl_add_u64 v[246:247], s[94:95], 0, v[186:187]
	s_setprio 1
	s_waitcnt lgkmcnt(11)
	v_mfma_f32_16x16x32_bf16 v[160:163], v[164:167], v[210:213], v[160:163]
	v_mfma_f32_16x16x32_bf16 v[156:159], v[172:175], v[210:213], v[156:159]
	s_waitcnt lgkmcnt(10)
	v_mfma_f32_16x16x32_bf16 v[152:155], v[164:167], v[218:221], v[152:155]
	v_mfma_f32_16x16x32_bf16 v[148:151], v[172:175], v[218:221], v[148:151]
	s_waitcnt lgkmcnt(9)
	v_mfma_f32_16x16x32_bf16 v[136:139], v[164:167], v[228:231], v[136:139]
	v_mfma_f32_16x16x32_bf16 v[132:135], v[172:175], v[228:231], v[132:135]
	s_waitcnt lgkmcnt(8)
	v_mfma_f32_16x16x32_bf16 v[120:123], v[164:167], v[236:239], v[120:123]
	v_mfma_f32_16x16x32_bf16 v[116:119], v[172:175], v[236:239], v[116:119]
	ds_read_b64_tr_b16 v[164:165], v190 offset:49152
	ds_read_b64_tr_b16 v[166:167], v191 offset:49152
	ds_read_b64_tr_b16 v[172:173], v192 offset:49152
	ds_read_b64_tr_b16 v[174:175], v193 offset:49152
	s_waitcnt lgkmcnt(7)
	v_mfma_f32_16x16x32_bf16 v[160:163], v[168:171], v[214:217], v[160:163]
	v_mfma_f32_16x16x32_bf16 v[156:159], v[176:179], v[214:217], v[156:159]
	s_waitcnt lgkmcnt(6)
	v_mfma_f32_16x16x32_bf16 v[152:155], v[168:171], v[224:227], v[152:155]
	v_mfma_f32_16x16x32_bf16 v[148:151], v[176:179], v[224:227], v[148:151]
	s_waitcnt lgkmcnt(5)
	v_mfma_f32_16x16x32_bf16 v[136:139], v[168:171], v[232:235], v[136:139]
	v_mfma_f32_16x16x32_bf16 v[132:135], v[176:179], v[232:235], v[132:135]
	s_waitcnt lgkmcnt(4)
	v_mfma_f32_16x16x32_bf16 v[120:123], v[168:171], v[240:243], v[120:123]
	v_mfma_f32_16x16x32_bf16 v[116:119], v[176:179], v[240:243], v[116:119]
	ds_read_b64_tr_b16 v[168:169], v190 offset:57344
	ds_read_b64_tr_b16 v[170:171], v191 offset:57344
	ds_read_b64_tr_b16 v[176:177], v192 offset:57344
	ds_read_b64_tr_b16 v[178:179], v193 offset:57344
	s_waitcnt lgkmcnt(4)
	v_mfma_f32_16x16x32_bf16 v[144:147], v[164:167], v[210:213], v[144:147]
	v_mfma_f32_16x16x32_bf16 v[140:143], v[172:175], v[210:213], v[140:143]
	ds_read_b128 v[210:213], v207 offset:49152
	v_mfma_f32_16x16x32_bf16 v[128:131], v[164:167], v[218:221], v[128:131]
	v_mfma_f32_16x16x32_bf16 v[124:127], v[172:175], v[218:221], v[124:127]
	ds_read_b128 v[218:221], v207 offset:51200
	v_mfma_f32_16x16x32_bf16 v[112:115], v[164:167], v[228:231], v[112:115]
	v_mfma_f32_16x16x32_bf16 v[108:111], v[172:175], v[228:231], v[108:111]
	ds_read_b128 v[228:231], v207 offset:53248
	v_mfma_f32_16x16x32_bf16 v[104:107], v[164:167], v[236:239], v[104:107]
	v_mfma_f32_16x16x32_bf16 v[100:103], v[172:175], v[236:239], v[100:103]
	ds_read_b128 v[236:239], v207 offset:55296
	ds_read_b64_tr_b16 v[164:165], v190 offset:32768
	ds_read_b64_tr_b16 v[166:167], v191 offset:32768
	ds_read_b64_tr_b16 v[172:173], v192 offset:32768
	ds_read_b64_tr_b16 v[174:175], v193 offset:32768
	s_waitcnt lgkmcnt(8)
	v_mfma_f32_16x16x32_bf16 v[144:147], v[168:171], v[214:217], v[144:147]
	v_mfma_f32_16x16x32_bf16 v[140:143], v[176:179], v[214:217], v[140:143]
	ds_read_b128 v[214:217], v207 offset:50176
	v_mfma_f32_16x16x32_bf16 v[128:131], v[168:171], v[224:227], v[128:131]
	v_mfma_f32_16x16x32_bf16 v[124:127], v[176:179], v[224:227], v[124:127]
	ds_read_b128 v[224:227], v207 offset:52224
	v_mfma_f32_16x16x32_bf16 v[112:115], v[168:171], v[232:235], v[112:115]
	v_mfma_f32_16x16x32_bf16 v[108:111], v[176:179], v[232:235], v[108:111]
	ds_read_b128 v[232:235], v207 offset:54272
	v_mfma_f32_16x16x32_bf16 v[104:107], v[168:171], v[240:243], v[104:107]
	v_mfma_f32_16x16x32_bf16 v[100:103], v[176:179], v[240:243], v[100:103]
	ds_read_b128 v[240:243], v207 offset:56320
	ds_read_b64_tr_b16 v[168:169], v190 offset:40960
	ds_read_b64_tr_b16 v[170:171], v191 offset:40960
	ds_read_b64_tr_b16 v[176:177], v192 offset:40960
	ds_read_b64_tr_b16 v[178:179], v193 offset:40960
	s_waitcnt lgkmcnt(8)
	v_mfma_f32_16x16x32_bf16 v[80:83], v[164:167], v[210:213], v[80:83]
	v_mfma_f32_16x16x32_bf16 v[68:71], v[172:175], v[210:213], v[68:71]
	v_mfma_f32_16x16x32_bf16 v[48:51], v[164:167], v[218:221], v[48:51]
	v_mfma_f32_16x16x32_bf16 v[44:47], v[172:175], v[218:221], v[44:47]
	v_mfma_f32_16x16x32_bf16 v[32:35], v[164:167], v[228:231], v[32:35]
	v_mfma_f32_16x16x32_bf16 v[28:31], v[172:175], v[228:231], v[28:31]
	v_mfma_f32_16x16x32_bf16 v[16:19], v[164:167], v[236:239], v[16:19]
	v_mfma_f32_16x16x32_bf16 v[12:15], v[172:175], v[236:239], v[12:15]
	ds_read_b64_tr_b16 v[164:165], v190 offset:49152
	ds_read_b64_tr_b16 v[166:167], v191 offset:49152
	ds_read_b64_tr_b16 v[172:173], v192 offset:49152
	ds_read_b64_tr_b16 v[174:175], v193 offset:49152
	s_waitcnt lgkmcnt(4)
	v_mfma_f32_16x16x32_bf16 v[80:83], v[168:171], v[214:217], v[80:83]
	v_mfma_f32_16x16x32_bf16 v[68:71], v[176:179], v[214:217], v[68:71]
	v_mfma_f32_16x16x32_bf16 v[48:51], v[168:171], v[224:227], v[48:51]
	v_mfma_f32_16x16x32_bf16 v[44:47], v[176:179], v[224:227], v[44:47]
	v_mfma_f32_16x16x32_bf16 v[32:35], v[168:171], v[232:235], v[32:35]
	v_mfma_f32_16x16x32_bf16 v[28:31], v[176:179], v[232:235], v[28:31]
	v_mfma_f32_16x16x32_bf16 v[16:19], v[168:171], v[240:243], v[16:19]
	v_mfma_f32_16x16x32_bf16 v[12:15], v[176:179], v[240:243], v[12:15]
	ds_read_b64_tr_b16 v[168:169], v190 offset:57344
	ds_read_b64_tr_b16 v[170:171], v191 offset:57344
	ds_read_b64_tr_b16 v[176:177], v192 offset:57344
	ds_read_b64_tr_b16 v[178:179], v193 offset:57344
	s_waitcnt lgkmcnt(4)
	v_mfma_f32_16x16x32_bf16 v[56:59], v[164:167], v[210:213], v[56:59]
	v_mfma_f32_16x16x32_bf16 v[52:55], v[172:175], v[210:213], v[52:55]
	s_waitcnt vmcnt(9)
	v_cvt_pk_bf16_f32 v244, v64, v65
	v_cvt_pk_bf16_f32 v245, v66, v67
	ds_write_b64 v196, v[244:245] offset:16384
	global_load_dwordx4 v[64:67], v189, s[2:3]
	v_mfma_f32_16x16x32_bf16 v[40:43], v[164:167], v[218:221], v[40:43]
	v_mfma_f32_16x16x32_bf16 v[36:39], v[172:175], v[218:221], v[36:39]
	s_waitcnt vmcnt(9)
	v_cvt_pk_bf16_f32 v244, v60, v61
	v_cvt_pk_bf16_f32 v245, v62, v63
	ds_write_b64 v197, v[244:245] offset:16384
	global_load_dwordx4 v[60:63], v189, s[48:49]
	v_mfma_f32_16x16x32_bf16 v[24:27], v[164:167], v[228:231], v[24:27]
	v_mfma_f32_16x16x32_bf16 v[20:23], v[172:175], v[228:231], v[20:23]
	s_waitcnt vmcnt(9)
	v_cvt_pk_bf16_f32 v244, v76, v77
	v_cvt_pk_bf16_f32 v245, v78, v79
	ds_write_b64 v195, v[244:245] offset:16384
	s_add_u32 s98, s2, 0x4000
	s_addc_u32 s99, s3, 0
	global_load_dwordx4 v[76:79], v189, s[98:99]
	v_mfma_f32_16x16x32_bf16 v[8:11], v[164:167], v[236:239], v[8:11]
	v_mfma_f32_16x16x32_bf16 v[2:5], v[172:175], v[236:239], v[4:7]
	s_waitcnt vmcnt(9)
	v_cvt_pk_bf16_f32 v244, v72, v73
	v_cvt_pk_bf16_f32 v245, v74, v75
	ds_write_b64 v197, v[244:245]
	s_add_u32 s100, s48, 0x4000
	s_addc_u32 s101, s49, 0
	global_load_dwordx4 v[72:75], v189, s[100:101]
	s_waitcnt lgkmcnt(4)
	v_mfma_f32_16x16x32_bf16 v[56:59], v[168:171], v[214:217], v[56:59]
	v_mfma_f32_16x16x32_bf16 v[52:55], v[176:179], v[214:217], v[52:55]
	s_waitcnt vmcnt(9)
	v_cvt_pk_bf16_f32 v244, v88, v89
	v_cvt_pk_bf16_f32 v245, v90, v91
	ds_write_b64 v194, v[244:245] offset:16384
	s_add_u32 s98, s2, 0x8000
	s_addc_u32 s99, s3, 0
	global_load_dwordx4 v[88:91], v189, s[98:99]
	v_mfma_f32_16x16x32_bf16 v[40:43], v[168:171], v[224:227], v[40:43]
	v_mfma_f32_16x16x32_bf16 v[36:39], v[176:179], v[224:227], v[36:39]
	s_waitcnt vmcnt(9)
	v_cvt_pk_bf16_f32 v244, v84, v85
	v_cvt_pk_bf16_f32 v245, v86, v87
	ds_write_b64 v196, v[244:245]
	s_add_u32 s100, s48, 0x8000
	s_addc_u32 s101, s49, 0
	global_load_dwordx4 v[84:87], v189, s[100:101]
	v_mfma_f32_16x16x32_bf16 v[24:27], v[168:171], v[232:235], v[24:27]
	v_mfma_f32_16x16x32_bf16 v[20:23], v[176:179], v[232:235], v[20:23]
	s_waitcnt vmcnt(9)
	v_cvt_pk_bf16_f32 v244, v96, v97
	v_cvt_pk_bf16_f32 v245, v98, v99
	ds_write_b64 v194, v[244:245]
	s_add_u32 s98, s2, 0xc000
	s_addc_u32 s99, s3, 0
	global_load_dwordx4 v[96:99], v189, s[98:99]
	v_mfma_f32_16x16x32_bf16 v[8:11], v[168:171], v[240:243], v[8:11]
	v_mfma_f32_16x16x32_bf16 v[4:7], v[176:179], v[240:243], v[2:5]
	s_waitcnt vmcnt(9)
	v_cvt_pk_bf16_f32 v244, v92, v93
	v_cvt_pk_bf16_f32 v245, v94, v95
	ds_write_b64 v195, v[244:245]
	s_add_u32 s100, s48, 0xc000
	s_addc_u32 s101, s49, 0
	global_load_dwordx4 v[92:95], v189, s[100:101]
	s_setprio 0
	s_branch .Lswp_dnO_tail
